# grid barrier: every workgroup starts an L2 write-back at arrival (non-blocking) so the XCD leader's write-back has little left
# baseline (speedup 1.0000x reference)
.LBB0_69:
	s_lshl_b32 s4, s33, 8
	s_add_u32 s4, s14, s4
	s_addc_u32 s5, s15, 0
	v_mov_b32_e32 v2, 0x1000
	v_mov_b32_e32 v4, 1
	global_atomic_add v4, v2, v4, s[4:5] offset:1024 sc0
	buffer_wbl2 sc1
	buffer_inv sc1
	v_cvt_f32_u32_e32 v2, v3
	v_sub_u32_e32 v5, 0, v3
	v_rcp_iflag_f32_e32 v2, v2
	s_nop 0
	v_mul_f32_e32 v2, 0x4f7ffffe, v2
	v_cvt_u32_f32_e32 v2, v2
	v_mul_lo_u32 v5, v5, v2
	v_mul_hi_u32 v5, v2, v5
	v_add_u32_e32 v2, v2, v5
	s_waitcnt vmcnt(2)
	v_mul_hi_u32 v2, v4, v2
	v_mul_lo_u32 v5, v2, v3
	v_sub_u32_e32 v5, v4, v5
	v_add_u32_e32 v6, 1, v2
	v_cmp_ge_u32_e32 vcc, v5, v3
	v_add_u32_e32 v4, 1, v4
	s_nop 0
	v_cndmask_b32_e32 v2, v2, v6, vcc
	v_sub_u32_e32 v6, v5, v3
	v_cndmask_b32_e32 v5, v5, v6, vcc
	v_add_u32_e32 v6, 1, v2
	v_cmp_ge_u32_e32 vcc, v5, v3
	s_nop 1
	v_cndmask_b32_e32 v2, v2, v6, vcc
	v_mul_lo_u32 v5, v3, v2
	v_add_u32_e32 v3, v5, v3
	v_cmp_ne_u32_e32 vcc, v4, v3
	s_and_saveexec_b64 s[6:7], vcc
	s_xor_b64 s[6:7], exec, s[6:7]
	s_cbranch_execz .LBB0_83
	s_waitcnt lgkmcnt(0)
	v_mov_b32_e32 v1, 0x2000
	global_load_dword v1, v1, s[4:5] offset:1024 sc1
	s_add_u32 s12, s4, 0x2400
	s_addc_u32 s13, s5, 0
	s_waitcnt vmcnt(0)
	v_cmp_eq_u32_e32 vcc, v1, v2
	s_and_saveexec_b64 s[8:9], vcc
	s_cbranch_execz .LBB0_82
	s_add_u32 s10, s16, 0x4200
	s_addc_u32 s11, s17, 0
	s_mov_b32 s34, 1
	s_mov_b64 s[22:23], 0
	v_mov_b32_e32 v1, 0
	s_branch .LBB0_73

.LBB0_170:
	v_readlane_b32 s4, v253, 8
	v_readlane_b32 s5, v253, 9
	v_cvt_f32_u32_e32 v1, v4
	v_sub_u32_e32 v6, 0, v4
	v_rcp_iflag_f32_e32 v1, v1
	s_nop 1
	global_atomic_add v5, v3, v228, s[4:5] sc0
	buffer_wbl2 sc1
	buffer_inv sc1
	v_mul_f32_e32 v1, 0x4f7ffffe, v1
	v_cvt_u32_f32_e32 v1, v1
	v_mul_lo_u32 v6, v6, v1
	v_mul_hi_u32 v6, v1, v6
	v_add_u32_e32 v1, v1, v6
	s_waitcnt vmcnt(2)
	v_mul_hi_u32 v1, v5, v1
	v_mul_lo_u32 v6, v1, v4
	v_sub_u32_e32 v6, v5, v6
	v_add_u32_e32 v7, 1, v1
	v_cmp_ge_u32_e32 vcc, v6, v4
	v_add_u32_e32 v5, 1, v5
	s_nop 0
	v_cndmask_b32_e32 v1, v1, v7, vcc
	v_sub_u32_e32 v7, v6, v4
	v_cndmask_b32_e32 v6, v6, v7, vcc
	v_add_u32_e32 v7, 1, v1
	v_cmp_ge_u32_e32 vcc, v6, v4
	s_nop 1
	v_cndmask_b32_e32 v1, v1, v7, vcc
	v_mul_lo_u32 v6, v4, v1
	v_add_u32_e32 v4, v6, v4
	v_cmp_ne_u32_e32 vcc, v5, v4
	s_and_saveexec_b64 s[4:5], vcc
	s_xor_b64 s[4:5], exec, s[4:5]
	s_cbranch_execz .LBB0_184
	v_readlane_b32 s6, v253, 10
	v_readlane_b32 s7, v253, 11
	s_waitcnt lgkmcnt(0)
	s_nop 3
	global_load_dword v2, v3, s[6:7] sc1
	s_waitcnt vmcnt(0)
	v_cmp_eq_u32_e32 vcc, v2, v1
	s_and_saveexec_b64 s[6:7], vcc
	s_cbranch_execz .LBB0_183
	s_mov_b32 s40, 1
	s_mov_b64 s[8:9], 0
	s_branch .LBB0_174

.LBB0_320:
	v_readlane_b32 s4, v253, 8
	v_readlane_b32 s5, v253, 9
	v_cvt_f32_u32_e32 v1, v4
	v_sub_u32_e32 v6, 0, v4
	v_rcp_iflag_f32_e32 v1, v1
	s_nop 1
	global_atomic_add v5, v3, v228, s[4:5] sc0
	buffer_wbl2 sc1
	buffer_inv sc1
	v_mul_f32_e32 v1, 0x4f7ffffe, v1
	v_cvt_u32_f32_e32 v1, v1
	v_mul_lo_u32 v6, v6, v1
	v_mul_hi_u32 v6, v1, v6
	v_add_u32_e32 v1, v1, v6
	s_waitcnt vmcnt(2)
	v_mul_hi_u32 v1, v5, v1
	v_mul_lo_u32 v6, v1, v4
	v_sub_u32_e32 v6, v5, v6
	v_add_u32_e32 v7, 1, v1
	v_cmp_ge_u32_e32 vcc, v6, v4
	v_add_u32_e32 v5, 1, v5
	s_nop 0
	v_cndmask_b32_e32 v1, v1, v7, vcc
	v_sub_u32_e32 v7, v6, v4
	v_cndmask_b32_e32 v6, v6, v7, vcc
	v_add_u32_e32 v7, 1, v1
	v_cmp_ge_u32_e32 vcc, v6, v4
	s_nop 1
	v_cndmask_b32_e32 v1, v1, v7, vcc
	v_mul_lo_u32 v6, v4, v1
	v_add_u32_e32 v4, v6, v4
	v_cmp_ne_u32_e32 vcc, v5, v4
	s_and_saveexec_b64 s[4:5], vcc
	s_xor_b64 s[4:5], exec, s[4:5]
	s_cbranch_execz .LBB0_334
	v_readlane_b32 s6, v253, 10
	v_readlane_b32 s7, v253, 11
	s_waitcnt lgkmcnt(0)
	s_nop 3
	global_load_dword v2, v3, s[6:7] sc1
	s_waitcnt vmcnt(0)
	v_cmp_eq_u32_e32 vcc, v2, v1
	s_and_saveexec_b64 s[6:7], vcc
	s_cbranch_execz .LBB0_333
	s_mov_b32 s33, 1
	s_mov_b64 s[8:9], 0
	s_branch .LBB0_324

.LBB0_524:
	v_readlane_b32 s4, v253, 8
	v_readlane_b32 s5, v253, 9
	v_cvt_f32_u32_e32 v1, v4
	v_sub_u32_e32 v6, 0, v4
	v_rcp_iflag_f32_e32 v1, v1
	s_nop 1
	global_atomic_add v5, v3, v228, s[4:5] sc0
	buffer_wbl2 sc1
	buffer_inv sc1
	v_mul_f32_e32 v1, 0x4f7ffffe, v1
	v_cvt_u32_f32_e32 v1, v1
	v_mul_lo_u32 v6, v6, v1
	v_mul_hi_u32 v6, v1, v6
	v_add_u32_e32 v1, v1, v6
	s_waitcnt vmcnt(2)
	v_mul_hi_u32 v1, v5, v1
	v_mul_lo_u32 v6, v1, v4
	v_sub_u32_e32 v6, v5, v6
	v_add_u32_e32 v7, 1, v1
	v_cmp_ge_u32_e32 vcc, v6, v4
	v_add_u32_e32 v5, 1, v5
	s_nop 0
	v_cndmask_b32_e32 v1, v1, v7, vcc
	v_sub_u32_e32 v7, v6, v4
	v_cndmask_b32_e32 v6, v6, v7, vcc
	v_add_u32_e32 v7, 1, v1
	v_cmp_ge_u32_e32 vcc, v6, v4
	s_nop 1
	v_cndmask_b32_e32 v1, v1, v7, vcc
	v_mul_lo_u32 v6, v4, v1
	v_add_u32_e32 v4, v6, v4
	v_cmp_ne_u32_e32 vcc, v5, v4
	s_and_saveexec_b64 s[4:5], vcc
	s_xor_b64 s[4:5], exec, s[4:5]
	s_cbranch_execz .LBB0_538
	v_readlane_b32 s6, v253, 10
	v_readlane_b32 s7, v253, 11
	s_waitcnt lgkmcnt(0)
	s_nop 3
	global_load_dword v2, v3, s[6:7] sc1
	s_waitcnt vmcnt(0)
	v_cmp_eq_u32_e32 vcc, v2, v1
	s_and_saveexec_b64 s[6:7], vcc
	s_cbranch_execz .LBB0_537
	s_mov_b32 s34, 1
	s_mov_b64 s[8:9], 0
	s_branch .LBB0_528
